# router logits GEMM: each wave covers both 16-token tiles over one K-eighth (table fragment reused for two MFMAs, table read once per workgroup), partials combined in LDS, double-buffered loads
# baseline (speedup 1.0000x reference)
.LBB0_1082:
	s_barrier
	s_and_saveexec_b64 s[6:7], s[0:1]
	ds_write_b32 v23, v27 offset:45056
	s_or_b64 exec, exec, s[6:7]
	s_mul_i32 s46, s34, s33
	s_add_i32 s46, s46, s2
	s_cmpk_lt_i32 s46, 0x100
	s_cselect_b64 s[26:27], -1, 0
	s_cmpk_gt_i32 s46, 0xff
	s_mov_b64 s[6:7], 0
	s_cbranch_scc1 .LBB0_1090
	v_ashrrev_i32_e32 v33, 31, v32
	v_lshlrev_b64 v[2:3], 13, v[32:33]
	v_mov_b32_e32 v26, 0
	v_lshl_add_u64 v[34:35], v[30:31], 0, v[2:3]
	v_mov_b32_e32 v2, 0
	v_mov_b32_e32 v3, v26
	v_mov_b32_e32 v4, v26
	v_mov_b32_e32 v5, v26
	v_mov_b32_e32 v10, 0
	v_mov_b32_e32 v11, v26
	v_mov_b32_e32 v12, v26
	v_mov_b32_e32 v13, v26
	v_mov_b32_e32 v6, 0
	v_mov_b32_e32 v7, v26
	v_mov_b32_e32 v8, v26
	v_mov_b32_e32 v9, v26
	v_mov_b32_e32 v14, 0
	v_mov_b32_e32 v15, v26
	v_mov_b32_e32 v16, v26
	v_mov_b32_e32 v17, v26
	v_mov_b32_e32 v18, 0
	v_mov_b32_e32 v19, v26
	v_mov_b32_e32 v20, v26
	v_mov_b32_e32 v21, v26
	s_lshr_b32 s98, s97, 2
	s_lshl_b32 s100, s98, 10
	s_lshl_b32 s101, s98, 17
	s_sub_u32 s99, s36, s101
	s_add_u32 s99, s99, s100
	v_add_co_u32_e32 v90, vcc, s99, v34
	s_add_u32 s99, s99, 0x20000
	s_nop 1
	v_addc_co_u32_e32 v91, vcc, 0, v35, vcc
	v_add_co_u32_e32 v92, vcc, s99, v34
	s_nop 1
	v_addc_co_u32_e32 v93, vcc, 0, v35, vcc
	s_add_u32 s99, s37, s100
	v_add_co_u32_e32 v94, vcc, s99, v28
	s_nop 1
	v_addc_co_u32_e32 v95, vcc, 0, v29, vcc
	s_add_u32 s99, s38, s100
	v_add_co_u32_e32 v96, vcc, s99, v28
	s_nop 1
	v_addc_co_u32_e32 v97, vcc, 0, v29, vcc
	s_add_u32 s99, s39, s100
	v_add_co_u32_e32 v98, vcc, s99, v28
	s_nop 1
	v_addc_co_u32_e32 v99, vcc, 0, v29, vcc
	s_add_u32 s99, s40, s100
	v_add_co_u32_e32 v100, vcc, s99, v28
	s_nop 1
	v_addc_co_u32_e32 v101, vcc, 0, v29, vcc
	s_add_u32 s99, s41, s100
	v_add_co_u32_e32 v102, vcc, s99, v28
	s_nop 1
	v_addc_co_u32_e32 v103, vcc, 0, v29, vcc
	s_mov_b64 s[98:99], 64
	v_mov_b32_e32 v33, 0
	v_mov_b32_e32 v70, 0
	v_mov_b32_e32 v71, 0
	v_mov_b32_e32 v72, 0
	v_mov_b32_e32 v73, 0
	v_mov_b32_e32 v74, 0
	v_mov_b32_e32 v75, 0
	v_mov_b32_e32 v76, 0
	v_mov_b32_e32 v77, 0
	v_mov_b32_e32 v78, 0
	v_mov_b32_e32 v79, 0
	v_mov_b32_e32 v80, 0
	v_mov_b32_e32 v81, 0
	v_mov_b32_e32 v82, 0
	v_mov_b32_e32 v83, 0
	v_mov_b32_e32 v84, 0
	v_mov_b32_e32 v85, 0
	v_mov_b32_e32 v86, 0
	v_mov_b32_e32 v87, 0
	v_mov_b32_e32 v88, 0
	v_mov_b32_e32 v89, 0
	s_mov_b32 s6, 0
	global_load_dwordx4 v[42:45], v[90:91], off
	global_load_dwordx4 v[46:49], v[92:93], off
	global_load_dwordx4 v[50:53], v[94:95], off
	global_load_dwordx4 v[54:57], v[96:97], off
	global_load_dwordx4 v[58:61], v[98:99], off
	global_load_dwordx4 v[62:65], v[100:101], off
	global_load_dwordx4 v[66:69], v[102:103], off
	v_lshl_add_u64 v[90:91], v[90:91], 0, s[98:99]
	v_lshl_add_u64 v[92:93], v[92:93], 0, s[98:99]
	v_lshl_add_u64 v[94:95], v[94:95], 0, s[98:99]
	v_lshl_add_u64 v[96:97], v[96:97], 0, s[98:99]
	v_lshl_add_u64 v[98:99], v[98:99], 0, s[98:99]
	v_lshl_add_u64 v[100:101], v[100:101], 0, s[98:99]
	v_lshl_add_u64 v[102:103], v[102:103], 0, s[98:99]
.Lrt2_loop:
	global_load_dwordx4 v[104:107], v[90:91], off
	global_load_dwordx4 v[108:111], v[92:93], off
	global_load_dwordx4 v[112:115], v[94:95], off
	global_load_dwordx4 v[116:119], v[96:97], off
	global_load_dwordx4 v[120:123], v[98:99], off
	global_load_dwordx4 v[124:127], v[100:101], off
	global_load_dwordx4 v[128:131], v[102:103], off
	v_lshl_add_u64 v[90:91], v[90:91], 0, s[98:99]
	v_lshl_add_u64 v[92:93], v[92:93], 0, s[98:99]
	v_lshl_add_u64 v[94:95], v[94:95], 0, s[98:99]
	v_lshl_add_u64 v[96:97], v[96:97], 0, s[98:99]
	v_lshl_add_u64 v[98:99], v[98:99], 0, s[98:99]
	v_lshl_add_u64 v[100:101], v[100:101], 0, s[98:99]
	v_lshl_add_u64 v[102:103], v[102:103], 0, s[98:99]
	s_waitcnt vmcnt(7)
	v_mfma_f32_16x16x4_f32 v[2:5], v42, v50, v[2:5]
	v_mfma_f32_16x16x4_f32 v[10:13], v42, v54, v[10:13]
	v_mfma_f32_16x16x4_f32 v[6:9], v42, v58, v[6:9]
	v_mfma_f32_16x16x4_f32 v[14:17], v42, v62, v[14:17]
	v_mfma_f32_16x16x4_f32 v[18:21], v42, v66, v[18:21]
	v_fmac_f32_e32 v26, v42, v42
	v_mfma_f32_16x16x4_f32 v[70:73], v46, v50, v[70:73]
	v_mfma_f32_16x16x4_f32 v[74:77], v46, v54, v[74:77]
	v_mfma_f32_16x16x4_f32 v[78:81], v46, v58, v[78:81]
	v_mfma_f32_16x16x4_f32 v[82:85], v46, v62, v[82:85]
	v_mfma_f32_16x16x4_f32 v[86:89], v46, v66, v[86:89]
	v_fmac_f32_e32 v33, v46, v46
	v_mfma_f32_16x16x4_f32 v[2:5], v43, v51, v[2:5]
	v_mfma_f32_16x16x4_f32 v[10:13], v43, v55, v[10:13]
	v_mfma_f32_16x16x4_f32 v[6:9], v43, v59, v[6:9]
	v_mfma_f32_16x16x4_f32 v[14:17], v43, v63, v[14:17]
	v_mfma_f32_16x16x4_f32 v[18:21], v43, v67, v[18:21]
	v_fmac_f32_e32 v26, v43, v43
	v_mfma_f32_16x16x4_f32 v[70:73], v47, v51, v[70:73]
	v_mfma_f32_16x16x4_f32 v[74:77], v47, v55, v[74:77]
	v_mfma_f32_16x16x4_f32 v[78:81], v47, v59, v[78:81]
	v_mfma_f32_16x16x4_f32 v[82:85], v47, v63, v[82:85]
	v_mfma_f32_16x16x4_f32 v[86:89], v47, v67, v[86:89]
	v_fmac_f32_e32 v33, v47, v47
	v_mfma_f32_16x16x4_f32 v[2:5], v44, v52, v[2:5]
	v_mfma_f32_16x16x4_f32 v[10:13], v44, v56, v[10:13]
	v_mfma_f32_16x16x4_f32 v[6:9], v44, v60, v[6:9]
	v_mfma_f32_16x16x4_f32 v[14:17], v44, v64, v[14:17]
	v_mfma_f32_16x16x4_f32 v[18:21], v44, v68, v[18:21]
	v_fmac_f32_e32 v26, v44, v44
	v_mfma_f32_16x16x4_f32 v[70:73], v48, v52, v[70:73]
	v_mfma_f32_16x16x4_f32 v[74:77], v48, v56, v[74:77]
	v_mfma_f32_16x16x4_f32 v[78:81], v48, v60, v[78:81]
	v_mfma_f32_16x16x4_f32 v[82:85], v48, v64, v[82:85]
	v_mfma_f32_16x16x4_f32 v[86:89], v48, v68, v[86:89]
	v_fmac_f32_e32 v33, v48, v48
	v_mfma_f32_16x16x4_f32 v[2:5], v45, v53, v[2:5]
	v_mfma_f32_16x16x4_f32 v[10:13], v45, v57, v[10:13]
	v_mfma_f32_16x16x4_f32 v[6:9], v45, v61, v[6:9]
	v_mfma_f32_16x16x4_f32 v[14:17], v45, v65, v[14:17]
	v_mfma_f32_16x16x4_f32 v[18:21], v45, v69, v[18:21]
	v_fmac_f32_e32 v26, v45, v45
	v_mfma_f32_16x16x4_f32 v[70:73], v49, v53, v[70:73]
	v_mfma_f32_16x16x4_f32 v[74:77], v49, v57, v[74:77]
	v_mfma_f32_16x16x4_f32 v[78:81], v49, v61, v[78:81]
	v_mfma_f32_16x16x4_f32 v[82:85], v49, v65, v[82:85]
	v_mfma_f32_16x16x4_f32 v[86:89], v49, v69, v[86:89]
	v_fmac_f32_e32 v33, v49, v49
	global_load_dwordx4 v[42:45], v[90:91], off
	global_load_dwordx4 v[46:49], v[92:93], off
	global_load_dwordx4 v[50:53], v[94:95], off
	global_load_dwordx4 v[54:57], v[96:97], off
	global_load_dwordx4 v[58:61], v[98:99], off
	global_load_dwordx4 v[62:65], v[100:101], off
	global_load_dwordx4 v[66:69], v[102:103], off
	v_lshl_add_u64 v[90:91], v[90:91], 0, s[98:99]
	v_lshl_add_u64 v[92:93], v[92:93], 0, s[98:99]
	v_lshl_add_u64 v[94:95], v[94:95], 0, s[98:99]
	v_lshl_add_u64 v[96:97], v[96:97], 0, s[98:99]
	v_lshl_add_u64 v[98:99], v[98:99], 0, s[98:99]
	v_lshl_add_u64 v[100:101], v[100:101], 0, s[98:99]
	v_lshl_add_u64 v[102:103], v[102:103], 0, s[98:99]
	s_waitcnt vmcnt(7)
	v_mfma_f32_16x16x4_f32 v[2:5], v104, v112, v[2:5]
	v_mfma_f32_16x16x4_f32 v[10:13], v104, v116, v[10:13]
	v_mfma_f32_16x16x4_f32 v[6:9], v104, v120, v[6:9]
	v_mfma_f32_16x16x4_f32 v[14:17], v104, v124, v[14:17]
	v_mfma_f32_16x16x4_f32 v[18:21], v104, v128, v[18:21]
	v_fmac_f32_e32 v26, v104, v104
	v_mfma_f32_16x16x4_f32 v[70:73], v108, v112, v[70:73]
	v_mfma_f32_16x16x4_f32 v[74:77], v108, v116, v[74:77]
	v_mfma_f32_16x16x4_f32 v[78:81], v108, v120, v[78:81]
	v_mfma_f32_16x16x4_f32 v[82:85], v108, v124, v[82:85]
	v_mfma_f32_16x16x4_f32 v[86:89], v108, v128, v[86:89]
	v_fmac_f32_e32 v33, v108, v108
	v_mfma_f32_16x16x4_f32 v[2:5], v105, v113, v[2:5]
	v_mfma_f32_16x16x4_f32 v[10:13], v105, v117, v[10:13]
	v_mfma_f32_16x16x4_f32 v[6:9], v105, v121, v[6:9]
	v_mfma_f32_16x16x4_f32 v[14:17], v105, v125, v[14:17]
	v_mfma_f32_16x16x4_f32 v[18:21], v105, v129, v[18:21]
	v_fmac_f32_e32 v26, v105, v105
	v_mfma_f32_16x16x4_f32 v[70:73], v109, v113, v[70:73]
	v_mfma_f32_16x16x4_f32 v[74:77], v109, v117, v[74:77]
	v_mfma_f32_16x16x4_f32 v[78:81], v109, v121, v[78:81]
	v_mfma_f32_16x16x4_f32 v[82:85], v109, v125, v[82:85]
	v_mfma_f32_16x16x4_f32 v[86:89], v109, v129, v[86:89]
	v_fmac_f32_e32 v33, v109, v109
	v_mfma_f32_16x16x4_f32 v[2:5], v106, v114, v[2:5]
	v_mfma_f32_16x16x4_f32 v[10:13], v106, v118, v[10:13]
	v_mfma_f32_16x16x4_f32 v[6:9], v106, v122, v[6:9]
	v_mfma_f32_16x16x4_f32 v[14:17], v106, v126, v[14:17]
	v_mfma_f32_16x16x4_f32 v[18:21], v106, v130, v[18:21]
	v_fmac_f32_e32 v26, v106, v106
	v_mfma_f32_16x16x4_f32 v[70:73], v110, v114, v[70:73]
	v_mfma_f32_16x16x4_f32 v[74:77], v110, v118, v[74:77]
	v_mfma_f32_16x16x4_f32 v[78:81], v110, v122, v[78:81]
	v_mfma_f32_16x16x4_f32 v[82:85], v110, v126, v[82:85]
	v_mfma_f32_16x16x4_f32 v[86:89], v110, v130, v[86:89]
	v_fmac_f32_e32 v33, v110, v110
	v_mfma_f32_16x16x4_f32 v[2:5], v107, v115, v[2:5]
	v_mfma_f32_16x16x4_f32 v[10:13], v107, v119, v[10:13]
	v_mfma_f32_16x16x4_f32 v[6:9], v107, v123, v[6:9]
	v_mfma_f32_16x16x4_f32 v[14:17], v107, v127, v[14:17]
	v_mfma_f32_16x16x4_f32 v[18:21], v107, v131, v[18:21]
	v_fmac_f32_e32 v26, v107, v107
	v_mfma_f32_16x16x4_f32 v[70:73], v111, v115, v[70:73]
	v_mfma_f32_16x16x4_f32 v[74:77], v111, v119, v[74:77]
	v_mfma_f32_16x16x4_f32 v[78:81], v111, v123, v[78:81]
	v_mfma_f32_16x16x4_f32 v[82:85], v111, v127, v[82:85]
	v_mfma_f32_16x16x4_f32 v[86:89], v111, v131, v[86:89]
	v_fmac_f32_e32 v33, v111, v111
	s_add_u32 s6, s6, 1
	s_cmp_eq_u32 s6, 8
	s_cbranch_scc0 .Lrt2_loop
	s_waitcnt vmcnt(0)
	s_nop 15
	s_nop 7
	s_lshr_b32 s100, s97, 2
	s_lshl_b32 s101, s100, 8
	v_subrev_u32_e32 v90, s101, v36
	s_mul_i32 s101, s100, 0x5000
	v_subrev_u32_e32 v91, s101, v25
	v_add_u32_e32 v92, 0x5000, v91
	v_mov_b32_e32 v93, v26
	v_mov_b32_e32 v94, v33
	s_nop 1
	v_permlane16_swap_b32 v26, v93
	v_permlane16_swap_b32 v33, v94
	s_nop 1
	v_add_f32_e32 v26, v26, v93
	v_add_f32_e32 v33, v33, v94
	v_mov_b32_e32 v93, v26
	v_mov_b32_e32 v94, v33
	s_nop 1
	v_permlane32_swap_b32 v26, v93
	v_permlane32_swap_b32 v33, v94
	s_nop 1
	v_add_f32_e32 v26, v26, v93
	v_add_f32_e32 v33, v33, v94
	s_cmp_eq_u32 s100, 0
	s_cbranch_scc0 .Lrt2_adder
	s_and_saveexec_b64 s[6:7], s[4:5]
	ds_write_b32 v90, v26 offset:40960
	ds_write_b32 v90, v33 offset:41216
	s_or_b64 exec, exec, s[6:7]
	ds_write_b32 v91, v2 offset:0
	ds_write_b32 v91, v3 offset:320
	ds_write_b32 v91, v4 offset:640
	ds_write_b32 v91, v5 offset:960
	ds_write_b32 v91, v10 offset:64
	ds_write_b32 v91, v11 offset:384
	ds_write_b32 v91, v12 offset:704
	ds_write_b32 v91, v13 offset:1024
	ds_write_b32 v91, v6 offset:128
	ds_write_b32 v91, v7 offset:448
	ds_write_b32 v91, v8 offset:768
	ds_write_b32 v91, v9 offset:1088
	ds_write_b32 v91, v14 offset:192
	ds_write_b32 v91, v15 offset:512
	ds_write_b32 v91, v16 offset:832
	ds_write_b32 v91, v17 offset:1152
	ds_write_b32 v91, v18 offset:256
	ds_write_b32 v91, v19 offset:576
	ds_write_b32 v91, v20 offset:896
	ds_write_b32 v91, v21 offset:1216
	ds_write_b32 v92, v70 offset:0
	ds_write_b32 v92, v71 offset:320
	ds_write_b32 v92, v72 offset:640
	ds_write_b32 v92, v73 offset:960
	ds_write_b32 v92, v74 offset:64
	ds_write_b32 v92, v75 offset:384
	ds_write_b32 v92, v76 offset:704
	ds_write_b32 v92, v77 offset:1024
	ds_write_b32 v92, v78 offset:128
	ds_write_b32 v92, v79 offset:448
	ds_write_b32 v92, v80 offset:768
	ds_write_b32 v92, v81 offset:1088
	ds_write_b32 v92, v82 offset:192
	ds_write_b32 v92, v83 offset:512
	ds_write_b32 v92, v84 offset:832
	ds_write_b32 v92, v85 offset:1152
	ds_write_b32 v92, v86 offset:256
	ds_write_b32 v92, v87 offset:576
	ds_write_b32 v92, v88 offset:896
	ds_write_b32 v92, v89 offset:1216
	s_waitcnt lgkmcnt(0)
	s_barrier
	s_branch .Lrt2_done
.Lrt2_adder:
	s_waitcnt lgkmcnt(0)
	s_barrier
	s_and_saveexec_b64 s[6:7], s[4:5]
	ds_add_f32 v90, v26 offset:40960
	ds_add_f32 v90, v33 offset:41216
	s_or_b64 exec, exec, s[6:7]
	ds_add_f32 v91, v2 offset:0
	ds_add_f32 v91, v3 offset:320
	ds_add_f32 v91, v4 offset:640
	ds_add_f32 v91, v5 offset:960
	ds_add_f32 v91, v10 offset:64
	ds_add_f32 v91, v11 offset:384
	ds_add_f32 v91, v12 offset:704
	ds_add_f32 v91, v13 offset:1024
	ds_add_f32 v91, v6 offset:128
	ds_add_f32 v91, v7 offset:448
	ds_add_f32 v91, v8 offset:768
	ds_add_f32 v91, v9 offset:1088
	ds_add_f32 v91, v14 offset:192
	ds_add_f32 v91, v15 offset:512
	ds_add_f32 v91, v16 offset:832
	ds_add_f32 v91, v17 offset:1152
	ds_add_f32 v91, v18 offset:256
	ds_add_f32 v91, v19 offset:576
	ds_add_f32 v91, v20 offset:896
	ds_add_f32 v91, v21 offset:1216
	ds_add_f32 v92, v70 offset:0
	ds_add_f32 v92, v71 offset:320
	ds_add_f32 v92, v72 offset:640
	ds_add_f32 v92, v73 offset:960
	ds_add_f32 v92, v74 offset:64
	ds_add_f32 v92, v75 offset:384
	ds_add_f32 v92, v76 offset:704
	ds_add_f32 v92, v77 offset:1024
	ds_add_f32 v92, v78 offset:128
	ds_add_f32 v92, v79 offset:448
	ds_add_f32 v92, v80 offset:768
	ds_add_f32 v92, v81 offset:1088
	ds_add_f32 v92, v82 offset:192
	ds_add_f32 v92, v83 offset:512
	ds_add_f32 v92, v84 offset:832
	ds_add_f32 v92, v85 offset:1152
	ds_add_f32 v92, v86 offset:256
	ds_add_f32 v92, v87 offset:576
	ds_add_f32 v92, v88 offset:896
	ds_add_f32 v92, v89 offset:1216
.Lrt2_done:
	s_mov_b64 s[6:7], s[22:23]
